# asymmetric final rendezvous in all four GEMM phases: waves 4-7 run their epilogue before the K-loop's final barrier, waves 0-3 after it
# speedup vs baseline: 1.0084x; 1.0037x over previous
; template <class Epi, class Sched>
; __device__ __forceinline__ void gemm_phase(LAS unsigned char* lds, const bf16_t* Abase, const int K, const Sched& S, const Epi& E, const int wvid) {
;     ...
;         E(acc, cur, wr, wc, fr, fq);
;         if (!has_next) break;
; #pragma unroll
;         for (int a = 0; a < 2; ++a)
; #pragma unroll
;             for (int b = 0; b < 2; ++b)
; #pragma unroll
;                 for (int m = 0; m < 4; ++m)
; #pragma unroll
;                     for (int n = 0; n < 2; ++n) acc[a][b][m][n] = (f32x4){0.f, 0.f, 0.f, 0.f};
;         cur = nxt; cB = nB; ++ui;
;     }
.LBB0_987:
	s_cmp_lt_u32 s74, 0x100
	s_cbranch_scc1 .Lxb3
	s_barrier

; __device__ __forceinline__ float bflo(unsigned w) { return __uint_as_float(w << 16); }
; __device__ __forceinline__ float bfhi(unsigned w) { return __uint_as_float(w & 0xFFFF0000u); }
; __device__ __forceinline__ unsigned cvt_pk_bf16(float lo, float hi) { f32x2c v = {lo, hi}; bf16x2c b = __builtin_convertvector(v, bf16x2c); return __builtin_bit_cast(unsigned, b); }
;     __device__ __forceinline__ void operator()(const f32x4 (&acc)[2][2][4][2], const Unit& u, int wr, int wc, int fr, int fq) const {
;         const int row0 = u.row0 + wr * 64 + fr, col0 = u.pn * BM + wc * 32 + 8 * fq;
;         if (u.kt * BK < Kfull) {
;             float* zp = ZP + ((size_t)u.e * BM + (wr * 64 + fr)) * D + col0;
; #pragma unroll
;             for (int ai = 0; ai < 2; ++ai)
; #pragma unroll
;                 for (int m = 0; m < 4; ++m)
; #pragma unroll
;                     for (int bj = 0; bj < 2; ++bj) { float* q = zp + (size_t)(ai * HALF + m * 16) * D + bj * HALF; *(f32x4*)q = acc[ai][bj][m][0]; *(f32x4*)(q + 4) = acc[ai][bj][m][1]; }
;             return;
;         }
; #pragma unroll
;         for (int ai = 0; ai < 2; ++ai)
; #pragma unroll
;             for (int m = 0; m < 4; ++m) { const size_t ro = (size_t)(row0 + ai * HALF + m * 16) * D + col0;
; #pragma unroll
;                 for (int bj = 0; bj < 2; ++bj) { const u32x4 h = *(const u32x4*)(hb + ro + bj * HALF); const f32x4 v0 = acc[ai][bj][m][0], v1 = acc[ai][bj][m][1];
;                     u32x4 w; w.x = cvt_pk_bf16(v0[0] + ALPHA * bflo(h.x), v0[1] + ALPHA * bfhi(h.x)); w.y = cvt_pk_bf16(v0[2] + ALPHA * bflo(h.y), v0[3] + ALPHA * bfhi(h.y));
;                     w.z = cvt_pk_bf16(v1[0] + ALPHA * bflo(h.z), v1[1] + ALPHA * bfhi(h.z)); w.w = cvt_pk_bf16(v1[2] + ALPHA * bflo(h.w), v1[3] + ALPHA * bfhi(h.w));
;                     *(u32x4*)(Z + ro + bj * HALF) = w; } }
.LBB0_1007:
	v_lshl_or_b32 v130, s22, 8, v189
	s_mov_b64 s[22:23], -1
	s_cmp_lt_i32 s57, 16
	v_ashrrev_i32_e32 v131, 31, v130
	s_cbranch_scc1 .Lgo_ks
	v_add_u32_e32 v132, s9, v188
	v_ashrrev_i32_e32 v133, 31, v132
	v_lshlrev_b64 v[132:133], 10, v[132:133]
	v_lshl_add_u64 v[132:133], v[132:133], 0, v[130:131]
	v_lshlrev_b64 v[132:133], 1, v[132:133]
	v_lshl_add_u64 v[138:139], s[4:5], 0, v[132:133]
	v_lshl_add_u64 v[140:141], s[2:3], 0, v[132:133]
	v_mov_b64_e32 v[142:143], v[138:139]
	global_load_dwordx4 v[144:147], v[142:143], off
	global_load_dwordx4 v[148:151], v[142:143], off offset:256
	v_add_co_u32_e32 v142, vcc, 0x8000, v142
	s_nop 1
	v_addc_co_u32_e32 v143, vcc, 0, v143, vcc
	global_load_dwordx4 v[152:155], v[142:143], off
	global_load_dwordx4 v[156:159], v[142:143], off offset:256
	v_add_co_u32_e32 v142, vcc, 0x8000, v142
	s_nop 1
	v_addc_co_u32_e32 v143, vcc, 0, v143, vcc
	global_load_dwordx4 v[160:163], v[142:143], off
	global_load_dwordx4 v[164:167], v[142:143], off offset:256
	v_add_co_u32_e32 v142, vcc, 0x8000, v142
	s_nop 1
	v_addc_co_u32_e32 v143, vcc, 0, v143, vcc
	global_load_dwordx4 v[168:171], v[142:143], off
	global_load_dwordx4 v[172:175], v[142:143], off offset:256
	v_add_co_u32_e32 v142, vcc, 0x28000, v142
	s_nop 1
	v_addc_co_u32_e32 v143, vcc, 0, v143, vcc
	s_cmp_lt_u32 s74, 0x100
	s_cbranch_scc0 .Lxa3
	s_barrier
.Lxa3:
	s_waitcnt vmcnt(7)
	v_lshlrev_b32_e32 v134, 16, v144
	v_and_b32_e32 v135, 0xffff0000, v144
	v_pk_fma_f32 v[134:135], v[134:135], s[88:89], v[126:127] op_sel_hi:[1,0,1]
	s_nop 0
	v_cvt_pk_bf16_f32 v144, v134, v135
	v_lshlrev_b32_e32 v134, 16, v145
	v_and_b32_e32 v135, 0xffff0000, v145
	v_pk_fma_f32 v[134:135], v[134:135], s[88:89], v[128:129] op_sel_hi:[1,0,1]
	s_nop 0
	v_cvt_pk_bf16_f32 v145, v134, v135
	v_lshlrev_b32_e32 v134, 16, v146
	v_and_b32_e32 v135, 0xffff0000, v146
	v_pk_fma_f32 v[134:135], v[134:135], s[88:89], v[122:123] op_sel_hi:[1,0,1]
	s_nop 0
	v_cvt_pk_bf16_f32 v146, v134, v135
	v_lshlrev_b32_e32 v134, 16, v147
	v_and_b32_e32 v135, 0xffff0000, v147
	v_pk_fma_f32 v[134:135], v[134:135], s[88:89], v[124:125] op_sel_hi:[1,0,1]
	s_nop 0
	v_cvt_pk_bf16_f32 v147, v134, v135
	global_store_dwordx4 v[140:141], v[144:147], off
	s_nop 1
	global_load_dwordx4 v[144:147], v[142:143], off
	s_waitcnt vmcnt(8)
	v_lshlrev_b32_e32 v134, 16, v148
	v_and_b32_e32 v135, 0xffff0000, v148
	v_pk_fma_f32 v[134:135], v[134:135], s[88:89], v[94:95] op_sel_hi:[1,0,1]
	s_nop 0
	v_cvt_pk_bf16_f32 v148, v134, v135
	v_lshlrev_b32_e32 v134, 16, v149
	v_and_b32_e32 v135, 0xffff0000, v149
	v_pk_fma_f32 v[134:135], v[134:135], s[88:89], v[96:97] op_sel_hi:[1,0,1]
	s_nop 0
	v_cvt_pk_bf16_f32 v149, v134, v135
	v_lshlrev_b32_e32 v134, 16, v150
	v_and_b32_e32 v135, 0xffff0000, v150
	v_pk_fma_f32 v[134:135], v[134:135], s[88:89], v[90:91] op_sel_hi:[1,0,1]
	s_nop 0
	v_cvt_pk_bf16_f32 v150, v134, v135
	v_lshlrev_b32_e32 v134, 16, v151
	v_and_b32_e32 v135, 0xffff0000, v151
	v_pk_fma_f32 v[134:135], v[134:135], s[88:89], v[92:93] op_sel_hi:[1,0,1]
	s_nop 0
	v_cvt_pk_bf16_f32 v151, v134, v135
	global_store_dwordx4 v[140:141], v[148:151], off offset:256
	v_add_co_u32_e32 v140, vcc, 0x8000, v140
	s_nop 1
	v_addc_co_u32_e32 v141, vcc, 0, v141, vcc
	global_load_dwordx4 v[148:151], v[142:143], off offset:256
	v_add_co_u32_e32 v142, vcc, 0x8000, v142
	s_nop 1
	v_addc_co_u32_e32 v143, vcc, 0, v143, vcc
	s_waitcnt vmcnt(9)
	v_lshlrev_b32_e32 v134, 16, v152
	v_and_b32_e32 v135, 0xffff0000, v152
	v_pk_fma_f32 v[134:135], v[134:135], s[88:89], v[118:119] op_sel_hi:[1,0,1]
	s_nop 0
	v_cvt_pk_bf16_f32 v152, v134, v135
	v_lshlrev_b32_e32 v134, 16, v153
	v_and_b32_e32 v135, 0xffff0000, v153
	v_pk_fma_f32 v[134:135], v[134:135], s[88:89], v[120:121] op_sel_hi:[1,0,1]
	s_nop 0
	v_cvt_pk_bf16_f32 v153, v134, v135
	v_lshlrev_b32_e32 v134, 16, v154
	v_and_b32_e32 v135, 0xffff0000, v154
	v_pk_fma_f32 v[134:135], v[134:135], s[88:89], v[114:115] op_sel_hi:[1,0,1]
	s_nop 0
	v_cvt_pk_bf16_f32 v154, v134, v135
	v_lshlrev_b32_e32 v134, 16, v155
	v_and_b32_e32 v135, 0xffff0000, v155
	v_pk_fma_f32 v[134:135], v[134:135], s[88:89], v[116:117] op_sel_hi:[1,0,1]
	s_nop 0
	v_cvt_pk_bf16_f32 v155, v134, v135
	global_store_dwordx4 v[140:141], v[152:155], off
	s_nop 1
	global_load_dwordx4 v[152:155], v[142:143], off
	s_waitcnt vmcnt(10)
	v_lshlrev_b32_e32 v134, 16, v156
	v_and_b32_e32 v135, 0xffff0000, v156
	v_pk_fma_f32 v[134:135], v[134:135], s[88:89], v[86:87] op_sel_hi:[1,0,1]
	s_nop 0
	v_cvt_pk_bf16_f32 v156, v134, v135
	v_lshlrev_b32_e32 v134, 16, v157
	v_and_b32_e32 v135, 0xffff0000, v157
	v_pk_fma_f32 v[134:135], v[134:135], s[88:89], v[88:89] op_sel_hi:[1,0,1]
	s_nop 0
	v_cvt_pk_bf16_f32 v157, v134, v135
	v_lshlrev_b32_e32 v134, 16, v158
	v_and_b32_e32 v135, 0xffff0000, v158
	v_pk_fma_f32 v[134:135], v[134:135], s[88:89], v[82:83] op_sel_hi:[1,0,1]
	s_nop 0
	v_cvt_pk_bf16_f32 v158, v134, v135
	v_lshlrev_b32_e32 v134, 16, v159
	v_and_b32_e32 v135, 0xffff0000, v159
	v_pk_fma_f32 v[134:135], v[134:135], s[88:89], v[84:85] op_sel_hi:[1,0,1]
	s_nop 0
	v_cvt_pk_bf16_f32 v159, v134, v135
	global_store_dwordx4 v[140:141], v[156:159], off offset:256
	v_add_co_u32_e32 v140, vcc, 0x8000, v140
	s_nop 1
	v_addc_co_u32_e32 v141, vcc, 0, v141, vcc
	global_load_dwordx4 v[156:159], v[142:143], off offset:256
	v_add_co_u32_e32 v142, vcc, 0x8000, v142
	s_nop 1
	v_addc_co_u32_e32 v143, vcc, 0, v143, vcc
	s_waitcnt vmcnt(11)
; __device__ __forceinline__ float bflo(unsigned w) { return __uint_as_float(w << 16); }
; __device__ __forceinline__ float bfhi(unsigned w) { return __uint_as_float(w & 0xFFFF0000u); }
; __device__ __forceinline__ unsigned cvt_pk_bf16(float lo, float hi) { f32x2c v = {lo, hi}; bf16x2c b = __builtin_convertvector(v, bf16x2c); return __builtin_bit_cast(unsigned, b); }
;     __device__ __forceinline__ void operator()(const f32x4 (&acc)[2][2][4][2], const Unit& u, int wr, int wc, int fr, int fq) const {
;     ...
;         for (int ai = 0; ai < 2; ++ai)
; #pragma unroll
;             for (int m = 0; m < 4; ++m) { const size_t ro = (size_t)(row0 + ai * HALF + m * 16) * D + col0;
; #pragma unroll
;                 for (int bj = 0; bj < 2; ++bj) { const u32x4 h = *(const u32x4*)(hb + ro + bj * HALF); const f32x4 v0 = acc[ai][bj][m][0], v1 = acc[ai][bj][m][1];
;                     u32x4 w; w.x = cvt_pk_bf16(v0[0] + ALPHA * bflo(h.x), v0[1] + ALPHA * bfhi(h.x)); w.y = cvt_pk_bf16(v0[2] + ALPHA * bflo(h.y), v0[3] + ALPHA * bfhi(h.y));
;                     w.z = cvt_pk_bf16(v1[0] + ALPHA * bflo(h.z), v1[1] + ALPHA * bfhi(h.z)); w.w = cvt_pk_bf16(v1[2] + ALPHA * bflo(h.w), v1[3] + ALPHA * bfhi(h.w));
;                     *(u32x4*)(Z + ro + bj * HALF) = w; } }
	v_lshlrev_b32_e32 v134, 16, v160
	v_and_b32_e32 v135, 0xffff0000, v160
	v_pk_fma_f32 v[134:135], v[134:135], s[88:89], v[110:111] op_sel_hi:[1,0,1]
	s_nop 0
	v_cvt_pk_bf16_f32 v160, v134, v135
	v_lshlrev_b32_e32 v134, 16, v161
	v_and_b32_e32 v135, 0xffff0000, v161
	v_pk_fma_f32 v[134:135], v[134:135], s[88:89], v[112:113] op_sel_hi:[1,0,1]
	s_nop 0
	v_cvt_pk_bf16_f32 v161, v134, v135
	v_lshlrev_b32_e32 v134, 16, v162
	v_and_b32_e32 v135, 0xffff0000, v162
	v_pk_fma_f32 v[134:135], v[134:135], s[88:89], v[106:107] op_sel_hi:[1,0,1]
	s_nop 0
	v_cvt_pk_bf16_f32 v162, v134, v135
	v_lshlrev_b32_e32 v134, 16, v163
	v_and_b32_e32 v135, 0xffff0000, v163
	v_pk_fma_f32 v[134:135], v[134:135], s[88:89], v[108:109] op_sel_hi:[1,0,1]
	s_nop 0
	v_cvt_pk_bf16_f32 v163, v134, v135
	global_store_dwordx4 v[140:141], v[160:163], off
	s_nop 1
	global_load_dwordx4 v[160:163], v[142:143], off
	s_waitcnt vmcnt(12)
	v_lshlrev_b32_e32 v134, 16, v164
	v_and_b32_e32 v135, 0xffff0000, v164
	v_pk_fma_f32 v[134:135], v[134:135], s[88:89], v[78:79] op_sel_hi:[1,0,1]
	s_nop 0
	v_cvt_pk_bf16_f32 v164, v134, v135
	v_lshlrev_b32_e32 v134, 16, v165
	v_and_b32_e32 v135, 0xffff0000, v165
	v_pk_fma_f32 v[134:135], v[134:135], s[88:89], v[80:81] op_sel_hi:[1,0,1]
	s_nop 0
	v_cvt_pk_bf16_f32 v165, v134, v135
	v_lshlrev_b32_e32 v134, 16, v166
	v_and_b32_e32 v135, 0xffff0000, v166
	v_pk_fma_f32 v[134:135], v[134:135], s[88:89], v[74:75] op_sel_hi:[1,0,1]
	s_nop 0
	v_cvt_pk_bf16_f32 v166, v134, v135
	v_lshlrev_b32_e32 v134, 16, v167
	v_and_b32_e32 v135, 0xffff0000, v167
	v_pk_fma_f32 v[134:135], v[134:135], s[88:89], v[76:77] op_sel_hi:[1,0,1]
	s_nop 0
	v_cvt_pk_bf16_f32 v167, v134, v135
	global_store_dwordx4 v[140:141], v[164:167], off offset:256
	v_add_co_u32_e32 v140, vcc, 0x8000, v140
	s_nop 1
	v_addc_co_u32_e32 v141, vcc, 0, v141, vcc
	global_load_dwordx4 v[164:167], v[142:143], off offset:256
	v_add_co_u32_e32 v142, vcc, 0x8000, v142
	s_nop 1
	v_addc_co_u32_e32 v143, vcc, 0, v143, vcc
	s_waitcnt vmcnt(13)
	v_lshlrev_b32_e32 v134, 16, v168
	v_and_b32_e32 v135, 0xffff0000, v168
	v_pk_fma_f32 v[134:135], v[134:135], s[88:89], v[102:103] op_sel_hi:[1,0,1]
	s_nop 0
	v_cvt_pk_bf16_f32 v168, v134, v135
	v_lshlrev_b32_e32 v134, 16, v169
	v_and_b32_e32 v135, 0xffff0000, v169
	v_pk_fma_f32 v[134:135], v[134:135], s[88:89], v[104:105] op_sel_hi:[1,0,1]
	s_nop 0
	v_cvt_pk_bf16_f32 v169, v134, v135
	v_lshlrev_b32_e32 v134, 16, v170
	v_and_b32_e32 v135, 0xffff0000, v170
	v_pk_fma_f32 v[134:135], v[134:135], s[88:89], v[98:99] op_sel_hi:[1,0,1]
	s_nop 0
	v_cvt_pk_bf16_f32 v170, v134, v135
	v_lshlrev_b32_e32 v134, 16, v171
	v_and_b32_e32 v135, 0xffff0000, v171
	v_pk_fma_f32 v[134:135], v[134:135], s[88:89], v[100:101] op_sel_hi:[1,0,1]
	s_nop 0
	v_cvt_pk_bf16_f32 v171, v134, v135
	global_store_dwordx4 v[140:141], v[168:171], off
	s_nop 1
	global_load_dwordx4 v[168:171], v[142:143], off
	s_waitcnt vmcnt(14)
	v_lshlrev_b32_e32 v134, 16, v172
	v_and_b32_e32 v135, 0xffff0000, v172
	v_pk_fma_f32 v[134:135], v[134:135], s[88:89], v[70:71] op_sel_hi:[1,0,1]
	s_nop 0
	v_cvt_pk_bf16_f32 v172, v134, v135
	v_lshlrev_b32_e32 v134, 16, v173
	v_and_b32_e32 v135, 0xffff0000, v173
	v_pk_fma_f32 v[134:135], v[134:135], s[88:89], v[72:73] op_sel_hi:[1,0,1]
	s_nop 0
	v_cvt_pk_bf16_f32 v173, v134, v135
	v_lshlrev_b32_e32 v134, 16, v174
	v_and_b32_e32 v135, 0xffff0000, v174
	v_pk_fma_f32 v[134:135], v[134:135], s[88:89], v[66:67] op_sel_hi:[1,0,1]
	s_nop 0
	v_cvt_pk_bf16_f32 v174, v134, v135
	v_lshlrev_b32_e32 v134, 16, v175
	v_and_b32_e32 v135, 0xffff0000, v175
	v_pk_fma_f32 v[134:135], v[134:135], s[88:89], v[68:69] op_sel_hi:[1,0,1]
	s_nop 0
	v_cvt_pk_bf16_f32 v175, v134, v135
	global_store_dwordx4 v[140:141], v[172:175], off offset:256
	v_add_co_u32_e32 v140, vcc, 0x28000, v140
	s_nop 1
	v_addc_co_u32_e32 v141, vcc, 0, v141, vcc
	global_load_dwordx4 v[172:175], v[142:143], off offset:256
	s_waitcnt vmcnt(14)
	v_lshlrev_b32_e32 v134, 16, v144
	v_and_b32_e32 v135, 0xffff0000, v144
	v_pk_fma_f32 v[134:135], v[134:135], s[88:89], v[62:63] op_sel_hi:[1,0,1]
	s_nop 0
	v_cvt_pk_bf16_f32 v144, v134, v135
	v_lshlrev_b32_e32 v134, 16, v145
	v_and_b32_e32 v135, 0xffff0000, v145
	v_pk_fma_f32 v[134:135], v[134:135], s[88:89], v[64:65] op_sel_hi:[1,0,1]
	s_nop 0
	v_cvt_pk_bf16_f32 v145, v134, v135
	v_lshlrev_b32_e32 v134, 16, v146
	v_and_b32_e32 v135, 0xffff0000, v146
	v_pk_fma_f32 v[134:135], v[134:135], s[88:89], v[58:59] op_sel_hi:[1,0,1]
	s_nop 0
	v_cvt_pk_bf16_f32 v146, v134, v135
	v_lshlrev_b32_e32 v134, 16, v147
	v_and_b32_e32 v135, 0xffff0000, v147
	v_pk_fma_f32 v[134:135], v[134:135], s[88:89], v[60:61] op_sel_hi:[1,0,1]
	s_nop 0
	v_cvt_pk_bf16_f32 v147, v134, v135
	global_store_dwordx4 v[140:141], v[144:147], off
	s_nop 1
	s_waitcnt vmcnt(13)
	v_lshlrev_b32_e32 v134, 16, v148
	v_and_b32_e32 v135, 0xffff0000, v148
	v_pk_fma_f32 v[134:135], v[134:135], s[88:89], v[46:47] op_sel_hi:[1,0,1]
	s_nop 0
	v_cvt_pk_bf16_f32 v148, v134, v135
	v_lshlrev_b32_e32 v134, 16, v149
	v_and_b32_e32 v135, 0xffff0000, v149
	v_pk_fma_f32 v[134:135], v[134:135], s[88:89], v[48:49] op_sel_hi:[1,0,1]
	s_nop 0
	v_cvt_pk_bf16_f32 v149, v134, v135
	v_lshlrev_b32_e32 v134, 16, v150
	v_and_b32_e32 v135, 0xffff0000, v150
	v_pk_fma_f32 v[134:135], v[134:135], s[88:89], v[38:39] op_sel_hi:[1,0,1]
	s_nop 0
	v_cvt_pk_bf16_f32 v150, v134, v135
	v_lshlrev_b32_e32 v134, 16, v151
	v_and_b32_e32 v135, 0xffff0000, v151
	v_pk_fma_f32 v[134:135], v[134:135], s[88:89], v[40:41] op_sel_hi:[1,0,1]
	s_nop 0
	v_cvt_pk_bf16_f32 v151, v134, v135
	global_store_dwordx4 v[140:141], v[148:151], off offset:256
	v_add_co_u32_e32 v140, vcc, 0x8000, v140
	s_nop 1
	v_addc_co_u32_e32 v141, vcc, 0, v141, vcc
	s_waitcnt vmcnt(12)
; __device__ __forceinline__ float bflo(unsigned w) { return __uint_as_float(w << 16); }
; __device__ __forceinline__ float bfhi(unsigned w) { return __uint_as_float(w & 0xFFFF0000u); }
; __device__ __forceinline__ unsigned cvt_pk_bf16(float lo, float hi) { f32x2c v = {lo, hi}; bf16x2c b = __builtin_convertvector(v, bf16x2c); return __builtin_bit_cast(unsigned, b); }
;     __device__ __forceinline__ void operator()(const f32x4 (&acc)[2][2][4][2], const Unit& u, int wr, int wc, int fr, int fq) const {
;     ...
;         for (int ai = 0; ai < 2; ++ai)
; #pragma unroll
;             for (int m = 0; m < 4; ++m) { const size_t ro = (size_t)(row0 + ai * HALF + m * 16) * D + col0;
; #pragma unroll
;                 for (int bj = 0; bj < 2; ++bj) { const u32x4 h = *(const u32x4*)(hb + ro + bj * HALF); const f32x4 v0 = acc[ai][bj][m][0], v1 = acc[ai][bj][m][1];
;                     u32x4 w; w.x = cvt_pk_bf16(v0[0] + ALPHA * bflo(h.x), v0[1] + ALPHA * bfhi(h.x)); w.y = cvt_pk_bf16(v0[2] + ALPHA * bflo(h.y), v0[3] + ALPHA * bfhi(h.y));
;                     w.z = cvt_pk_bf16(v1[0] + ALPHA * bflo(h.z), v1[1] + ALPHA * bfhi(h.z)); w.w = cvt_pk_bf16(v1[2] + ALPHA * bflo(h.w), v1[3] + ALPHA * bfhi(h.w));
;                     *(u32x4*)(Z + ro + bj * HALF) = w; } }
	v_lshlrev_b32_e32 v134, 16, v152
	v_and_b32_e32 v135, 0xffff0000, v152
	v_pk_fma_f32 v[134:135], v[134:135], s[88:89], v[54:55] op_sel_hi:[1,0,1]
	s_nop 0
	v_cvt_pk_bf16_f32 v152, v134, v135
	v_lshlrev_b32_e32 v134, 16, v153
	v_and_b32_e32 v135, 0xffff0000, v153
	v_pk_fma_f32 v[134:135], v[134:135], s[88:89], v[56:57] op_sel_hi:[1,0,1]
	s_nop 0
	v_cvt_pk_bf16_f32 v153, v134, v135
	v_lshlrev_b32_e32 v134, 16, v154
	v_and_b32_e32 v135, 0xffff0000, v154
	v_pk_fma_f32 v[134:135], v[134:135], s[88:89], v[50:51] op_sel_hi:[1,0,1]
	s_nop 0
	v_cvt_pk_bf16_f32 v154, v134, v135
	v_lshlrev_b32_e32 v134, 16, v155
	v_and_b32_e32 v135, 0xffff0000, v155
	v_pk_fma_f32 v[134:135], v[134:135], s[88:89], v[52:53] op_sel_hi:[1,0,1]
	s_nop 0
	v_cvt_pk_bf16_f32 v155, v134, v135
	global_store_dwordx4 v[140:141], v[152:155], off
	s_nop 1
	s_waitcnt vmcnt(11)
	v_lshlrev_b32_e32 v134, 16, v156
	v_and_b32_e32 v135, 0xffff0000, v156
	v_pk_fma_f32 v[134:135], v[134:135], s[88:89], v[30:31] op_sel_hi:[1,0,1]
	s_nop 0
	v_cvt_pk_bf16_f32 v156, v134, v135
	v_lshlrev_b32_e32 v134, 16, v157
	v_and_b32_e32 v135, 0xffff0000, v157
	v_pk_fma_f32 v[134:135], v[134:135], s[88:89], v[32:33] op_sel_hi:[1,0,1]
	s_nop 0
	v_cvt_pk_bf16_f32 v157, v134, v135
	v_lshlrev_b32_e32 v134, 16, v158
	v_and_b32_e32 v135, 0xffff0000, v158
	v_pk_fma_f32 v[134:135], v[134:135], s[88:89], v[22:23] op_sel_hi:[1,0,1]
	s_nop 0
	v_cvt_pk_bf16_f32 v158, v134, v135
	v_lshlrev_b32_e32 v134, 16, v159
	v_and_b32_e32 v135, 0xffff0000, v159
	v_pk_fma_f32 v[134:135], v[134:135], s[88:89], v[24:25] op_sel_hi:[1,0,1]
	s_nop 0
	v_cvt_pk_bf16_f32 v159, v134, v135
	global_store_dwordx4 v[140:141], v[156:159], off offset:256
	v_add_co_u32_e32 v140, vcc, 0x8000, v140
	s_nop 1
	v_addc_co_u32_e32 v141, vcc, 0, v141, vcc
	s_waitcnt vmcnt(10)
	v_lshlrev_b32_e32 v134, 16, v160
	v_and_b32_e32 v135, 0xffff0000, v160
	v_pk_fma_f32 v[134:135], v[134:135], s[88:89], v[42:43] op_sel_hi:[1,0,1]
	s_nop 0
	v_cvt_pk_bf16_f32 v160, v134, v135
	v_lshlrev_b32_e32 v134, 16, v161
	v_and_b32_e32 v135, 0xffff0000, v161
	v_pk_fma_f32 v[134:135], v[134:135], s[88:89], v[44:45] op_sel_hi:[1,0,1]
	s_nop 0
	v_cvt_pk_bf16_f32 v161, v134, v135
	v_lshlrev_b32_e32 v134, 16, v162
	v_and_b32_e32 v135, 0xffff0000, v162
	v_pk_fma_f32 v[134:135], v[134:135], s[88:89], v[34:35] op_sel_hi:[1,0,1]
	s_nop 0
	v_cvt_pk_bf16_f32 v162, v134, v135
	v_lshlrev_b32_e32 v134, 16, v163
	v_and_b32_e32 v135, 0xffff0000, v163
	v_pk_fma_f32 v[134:135], v[134:135], s[88:89], v[36:37] op_sel_hi:[1,0,1]
	s_nop 0
	v_cvt_pk_bf16_f32 v163, v134, v135
	global_store_dwordx4 v[140:141], v[160:163], off
	s_nop 1
	s_waitcnt vmcnt(9)
	v_lshlrev_b32_e32 v134, 16, v164
	v_and_b32_e32 v135, 0xffff0000, v164
	v_pk_fma_f32 v[134:135], v[134:135], s[88:89], v[14:15] op_sel_hi:[1,0,1]
	s_nop 0
	v_cvt_pk_bf16_f32 v164, v134, v135
	v_lshlrev_b32_e32 v134, 16, v165
	v_and_b32_e32 v135, 0xffff0000, v165
	v_pk_fma_f32 v[134:135], v[134:135], s[88:89], v[16:17] op_sel_hi:[1,0,1]
	s_nop 0
	v_cvt_pk_bf16_f32 v165, v134, v135
	v_lshlrev_b32_e32 v134, 16, v166
	v_and_b32_e32 v135, 0xffff0000, v166
	v_pk_fma_f32 v[134:135], v[134:135], s[88:89], v[10:11] op_sel_hi:[1,0,1]
	s_nop 0
	v_cvt_pk_bf16_f32 v166, v134, v135
	v_lshlrev_b32_e32 v134, 16, v167
	v_and_b32_e32 v135, 0xffff0000, v167
	v_pk_fma_f32 v[134:135], v[134:135], s[88:89], v[12:13] op_sel_hi:[1,0,1]
	s_nop 0
	v_cvt_pk_bf16_f32 v167, v134, v135
	global_store_dwordx4 v[140:141], v[164:167], off offset:256
	v_add_co_u32_e32 v140, vcc, 0x8000, v140
	s_nop 1
	v_addc_co_u32_e32 v141, vcc, 0, v141, vcc
	s_waitcnt vmcnt(8)
	v_lshlrev_b32_e32 v134, 16, v168
	v_and_b32_e32 v135, 0xffff0000, v168
	v_pk_fma_f32 v[134:135], v[134:135], s[88:89], v[26:27] op_sel_hi:[1,0,1]
	s_nop 0
	v_cvt_pk_bf16_f32 v168, v134, v135
	v_lshlrev_b32_e32 v134, 16, v169
	v_and_b32_e32 v135, 0xffff0000, v169
	v_pk_fma_f32 v[134:135], v[134:135], s[88:89], v[28:29] op_sel_hi:[1,0,1]
	s_nop 0
	v_cvt_pk_bf16_f32 v169, v134, v135
	v_lshlrev_b32_e32 v134, 16, v170
	v_and_b32_e32 v135, 0xffff0000, v170
	v_pk_fma_f32 v[134:135], v[134:135], s[88:89], v[18:19] op_sel_hi:[1,0,1]
	s_nop 0
	v_cvt_pk_bf16_f32 v170, v134, v135
	v_lshlrev_b32_e32 v134, 16, v171
	v_and_b32_e32 v135, 0xffff0000, v171
	v_pk_fma_f32 v[134:135], v[134:135], s[88:89], v[20:21] op_sel_hi:[1,0,1]
	s_nop 0
	v_cvt_pk_bf16_f32 v171, v134, v135
	global_store_dwordx4 v[140:141], v[168:171], off
	s_nop 1
	s_waitcnt vmcnt(7)
	v_lshlrev_b32_e32 v134, 16, v172
	v_and_b32_e32 v135, 0xffff0000, v172
	v_pk_fma_f32 v[134:135], v[134:135], s[88:89], v[6:7] op_sel_hi:[1,0,1]
	s_nop 0
	v_cvt_pk_bf16_f32 v172, v134, v135
	v_lshlrev_b32_e32 v134, 16, v173
	v_and_b32_e32 v135, 0xffff0000, v173
	v_pk_fma_f32 v[134:135], v[134:135], s[88:89], v[8:9] op_sel_hi:[1,0,1]
	s_nop 0
	v_cvt_pk_bf16_f32 v173, v134, v135
	v_lshlrev_b32_e32 v134, 16, v174
	v_and_b32_e32 v135, 0xffff0000, v174
	v_pk_fma_f32 v[134:135], v[134:135], s[88:89], v[2:3] op_sel_hi:[1,0,1]
	s_nop 0
	v_cvt_pk_bf16_f32 v174, v134, v135
	v_lshlrev_b32_e32 v134, 16, v175
	v_and_b32_e32 v135, 0xffff0000, v175
	v_pk_fma_f32 v[134:135], v[134:135], s[88:89], v[4:5] op_sel_hi:[1,0,1]
	s_nop 0
	v_cvt_pk_bf16_f32 v175, v134, v135
	global_store_dwordx4 v[140:141], v[172:175], off offset:256
	s_nop 1
	s_mov_b64 s[22:23], 0
	s_branch .LBB0_1009

;     __device__ __forceinline__ void operator()(const f32x4 (&acc)[2][2][4][2], const Unit& u, int wr, int wc, int fr, int fq) const {
;     ...
;         if (u.kt * BK < Kfull) {
;             float* zp = ZP + ((size_t)u.e * BM + (wr * 64 + fr)) * D + col0;
; #pragma unroll
;             for (int ai = 0; ai < 2; ++ai)
; #pragma unroll
;                 for (int m = 0; m < 4; ++m)
; #pragma unroll
;                     for (int bj = 0; bj < 2; ++bj) { float* q = zp + (size_t)(ai * HALF + m * 16) * D + bj * HALF; *(f32x4*)q = acc[ai][bj][m][0]; *(f32x4*)(q + 4) = acc[ai][bj][m][1]; }
;             return;
.Lxa4:
.LBB0_1009:
	s_andn2_b64 vcc, exec, s[22:23]
	s_cbranch_vccnz .LBB0_987
	s_ashr_i32 s9, s8, 31
	s_lshl_b64 s[8:9], s[8:9], 20
	v_lshl_add_u64 v[132:133], v[190:191], 0, s[8:9]
	v_lshl_add_u64 v[130:131], v[130:131], 2, v[132:133]
	global_store_dwordx4 v[130:131], v[126:129], off
	global_store_dwordx4 v[130:131], v[122:125], off offset:16
	global_store_dwordx4 v[130:131], v[94:97], off offset:512
	global_store_dwordx4 v[130:131], v[90:93], off offset:528
	s_mov_b32 s8, 0x80000
	s_nop 0
	v_add_co_u32_e32 v90, vcc, 0x10000, v130
	s_nop 1
	v_addc_co_u32_e32 v91, vcc, 0, v131, vcc
	global_store_dwordx4 v[90:91], v[118:121], off
	global_store_dwordx4 v[90:91], v[114:117], off offset:16
	global_store_dwordx4 v[90:91], v[86:89], off offset:512
	global_store_dwordx4 v[90:91], v[82:85], off offset:528
	s_nop 1
	v_add_co_u32_e32 v82, vcc, 0x20000, v130
	s_nop 1
	v_addc_co_u32_e32 v83, vcc, 0, v131, vcc
	global_store_dwordx4 v[82:83], v[110:113], off
	global_store_dwordx4 v[82:83], v[106:109], off offset:16
	global_store_dwordx4 v[82:83], v[78:81], off offset:512
	global_store_dwordx4 v[82:83], v[74:77], off offset:528
	s_nop 1
	v_add_co_u32_e32 v74, vcc, 0x30000, v130
	s_nop 1
	v_addc_co_u32_e32 v75, vcc, 0, v131, vcc
	global_store_dwordx4 v[74:75], v[102:105], off
	global_store_dwordx4 v[74:75], v[98:101], off offset:16
	global_store_dwordx4 v[74:75], v[70:73], off offset:512
	global_store_dwordx4 v[74:75], v[66:69], off offset:528
	s_nop 1
	v_add_co_u32_e32 v66, vcc, s8, v130
	s_nop 1
	v_addc_co_u32_e32 v67, vcc, 0, v131, vcc
	global_store_dwordx4 v[66:67], v[62:65], off
	global_store_dwordx4 v[66:67], v[58:61], off offset:16
	global_store_dwordx4 v[66:67], v[46:49], off offset:512
	global_store_dwordx4 v[66:67], v[38:41], off offset:528
	s_nop 1
	v_add_co_u32_e32 v38, vcc, 0x90000, v130
	s_nop 1
	v_addc_co_u32_e32 v39, vcc, 0, v131, vcc
	global_store_dwordx4 v[38:39], v[54:57], off
	global_store_dwordx4 v[38:39], v[50:53], off offset:16
	global_store_dwordx4 v[38:39], v[30:33], off offset:512
	global_store_dwordx4 v[38:39], v[22:25], off offset:528
	s_nop 1
	v_add_co_u32_e32 v22, vcc, 0xa0000, v130
	s_nop 1
	v_addc_co_u32_e32 v23, vcc, 0, v131, vcc
	global_store_dwordx4 v[22:23], v[42:45], off
	global_store_dwordx4 v[22:23], v[34:37], off offset:16
	global_store_dwordx4 v[22:23], v[14:17], off offset:512
	global_store_dwordx4 v[22:23], v[10:13], off offset:528
	s_nop 1
	v_add_co_u32_e32 v10, vcc, 0xb0000, v130
	s_nop 1
	v_addc_co_u32_e32 v11, vcc, 0, v131, vcc
	global_store_dwordx4 v[10:11], v[26:29], off
	global_store_dwordx4 v[10:11], v[18:21], off offset:16
	global_store_dwordx4 v[10:11], v[6:9], off offset:512
	global_store_dwordx4 v[10:11], v[2:5], off offset:528
	s_branch .LBB0_987

; template <class Epi, class Sched>
; __device__ __forceinline__ void gemm_phase(LAS unsigned char* lds, const bf16_t* Abase, const int K, const Sched& S, const Epi& E, const int wvid) {
;     ...
;         E(acc, cur, wr, wc, fr, fq);
;         if (!has_next) break;
; #pragma unroll
;         for (int a = 0; a < 2; ++a)
; #pragma unroll
;             for (int b = 0; b < 2; ++b)
; #pragma unroll
;                 for (int m = 0; m < 4; ++m)
; #pragma unroll
;                     for (int n = 0; n < 2; ++n) acc[a][b][m][n] = (f32x4){0.f, 0.f, 0.f, 0.f};
;         cur = nxt; cB = nB; ++ui;
.LBB0_1201:
	s_or_b64 exec, exec, s[0:1]
	s_cmp_lt_u32 s74, 0x100
	s_cbranch_scc1 .Lxb1
	s_barrier
.Lxb1:
	s_and_b64 vcc, exec, s[2:3]
	v_mov_b32_e32 v228, v227
	s_mov_b32 s24, s22
	v_mov_b32_e32 v179, v193
	v_mov_b64_e32 v[2:3], v[194:195]
	s_cbranch_vccnz .LBB0_1230

; #define PG8_STAGE(bufoff, gbase, voff) do { _Pragma("unroll") for (int _i = 0; _i < 2; ++_i) \
;         __builtin_amdgcn_global_load_lds((const unsigned*)((const char*)(gbase) + (voff)[_i]), (LAS unsigned*)(lds + (bufoff) + ldsw + _i * 8192), 16, 0, 0); } while (0)
; #define PG8_LDA(dst, b, h) do { _Pragma("unroll") for (int m = 0; m < 4; ++m) _Pragma("unroll") for (int k = 0; k < 2; ++k) dst[m][k] = *(const LAS bf16x8*)(lds + PG8_SA(b, h) + aoff + m * 2048 + k * 1024); } while (0)
; #define PG8_LDB(dst, b, h) do { _Pragma("unroll") for (int n = 0; n < 2; ++n) _Pragma("unroll") for (int k = 0; k < 2; ++k) dst[n][k] = *(const LAS bf16x8*)(lds + PG8_SB(b, h) + boff + n * 2048 + k * 1024); } while (0)
; #define PG8_MMA(ai, bj, At, Bt) do { __builtin_amdgcn_s_setprio(1); _Pragma("unroll") for (int m = 0; m < 4; ++m) _Pragma("unroll") for (int n = 0; n < 2; ++n) _Pragma("unroll") for (int k = 0; k < 2; ++k) \
;         acc[ai][bj][m][n] = __builtin_amdgcn_mfma_f32_16x16x32_bf16(Bt[n][k], At[m][k], acc[ai][bj][m][n], 0, 0, 0); __builtin_amdgcn_s_setprio(0); } while (0)
; #define PG8_WAIT_V(n) asm volatile("s_waitcnt vmcnt(" #n ")" ::: "memory")
; #define PG8_WAIT_L(n) asm volatile("s_waitcnt lgkmcnt(" #n ")" ::: "memory")
; #define PG8_BAR __builtin_amdgcn_s_barrier()
; #define PG8_SCHED __builtin_amdgcn_sched_barrier(0)
; template <class Epi, class Sched>
; __device__ __forceinline__ void gemm_phase(LAS unsigned char* lds, const bf16_t* Abase, const int K, const Sched& S, const Epi& E, const int wvid) {
;     ...
;             const char* a2 = last ? Ab : Ab + (size_t)(t + 2) * kstep; const char* b2 = last ? nB : cB + (size_t)(t + 2) * kstep;
;             const char* a3 = a2 + kstep; const char* b3 = b2 + kstep;
;             PG8_LDB(B1, 0, 1); PG8_STAGE(PG8_SB(0, 0), b2, voffB);
;             PG8_BAR; PG8_WAIT_L(0); PG8_MMA(0, 1, At, B1); PG8_BAR;
;             PG8_LDA(At, 0, 1); PG8_STAGE(PG8_SA(0, 0), a2, voffA[0]);
;             PG8_BAR; PG8_WAIT_L(0); PG8_MMA(1, 0, At, B0); PG8_BAR; PG8_SCHED;
;             PG8_STAGE(PG8_SB(0, 1), b2 + hstep, voffB);
;             PG8_WAIT_V(6); PG8_BAR; PG8_MMA(1, 1, At, B1); PG8_BAR;
;             PG8_LDB(B0, 1, 0); PG8_SCHED; PG8_LDA(At, 1, 0); PG8_STAGE(PG8_SA(0, 1), a2, voffA[1]);
;             PG8_WAIT_L(8); PG8_BAR; PG8_WAIT_L(0); PG8_MMA(0, 0, At, B0); PG8_BAR; PG8_SCHED;
.LBB0_1212:
	s_add_u32 s28, s26, 0x100
	s_addc_u32 s29, s27, 0
	s_and_b64 s[30:31], s[4:5], exec
	s_cselect_b32 s30, 0, s28
	s_cselect_b32 s31, 0, s29
	s_add_u32 s30, s16, s30
	v_lshl_add_u64 v[236:237], v[196:197], 0, s[26:27]
	s_addc_u32 s31, s17, s31
	s_add_i32 s26, 0, 0x14000
	v_cndmask_b32_e64 v237, v237, v191, s[4:5]
	v_cndmask_b32_e64 v236, v236, v229, s[4:5]
	s_mov_b32 m0, s39
	v_add_u32_e32 v185, s26, v224
	v_lshl_add_u64 v[238:239], v[236:237], 0, v[180:181]
	ds_read_b128 v[200:203], v185
	ds_read_b128 v[206:209], v185 offset:1024
	ds_read_b128 v[210:213], v185 offset:2048
	ds_read_b128 v[232:235], v185 offset:3072
	global_load_lds_dwordx4 v[238:239], off
	v_lshl_add_u64 v[240:241], v[236:237], 0, v[182:183]
	s_mov_b32 m0, s42
	s_nop 0
	global_load_lds_dwordx4 v[240:241], off
	s_barrier
	s_waitcnt lgkmcnt(0)
	s_waitcnt lgkmcnt(0)
	v_mfma_f32_16x16x32_bf16 v[102:105], v[200:203], v[170:173], v[102:105]
	v_mfma_f32_16x16x32_bf16 v[98:101], v[210:213], v[170:173], v[98:101]
	v_mfma_f32_16x16x32_bf16 v[86:89], v[200:203], v[162:165], v[86:89]
	v_mfma_f32_16x16x32_bf16 v[82:85], v[210:213], v[162:165], v[82:85]
	v_mfma_f32_16x16x32_bf16 v[78:81], v[200:203], v[154:157], v[78:81]
	v_mfma_f32_16x16x32_bf16 v[74:77], v[210:213], v[154:157], v[74:77]
	v_mfma_f32_16x16x32_bf16 v[70:73], v[200:203], v[146:149], v[70:73]
	v_mfma_f32_16x16x32_bf16 v[66:69], v[210:213], v[146:149], v[66:69]
	v_mfma_f32_16x16x32_bf16 v[102:105], v[206:209], v[174:177], v[102:105]
	v_mfma_f32_16x16x32_bf16 v[98:101], v[232:235], v[174:177], v[98:101]
	v_mfma_f32_16x16x32_bf16 v[86:89], v[206:209], v[166:169], v[86:89]
	v_mfma_f32_16x16x32_bf16 v[82:85], v[232:235], v[166:169], v[82:85]
	v_mfma_f32_16x16x32_bf16 v[78:81], v[206:209], v[158:161], v[78:81]
	v_mfma_f32_16x16x32_bf16 v[74:77], v[232:235], v[158:161], v[74:77]
	v_mfma_f32_16x16x32_bf16 v[70:73], v[206:209], v[150:153], v[70:73]
	v_mfma_f32_16x16x32_bf16 v[66:69], v[232:235], v[150:153], v[66:69]
	s_mov_b32 m0, s25
	s_barrier
	ds_read_b128 v[146:149], v226 offset:16384
	ds_read_b128 v[150:153], v226 offset:17408
	ds_read_b128 v[154:157], v226 offset:18432
	ds_read_b128 v[158:161], v226 offset:19456
	ds_read_b128 v[162:165], v226 offset:20480
	ds_read_b128 v[166:169], v226 offset:21504
	ds_read_b128 v[170:173], v226 offset:22528
	ds_read_b128 v[174:177], v226 offset:23552
	global_load_lds_dwordx4 v0, s[30:31]
	s_mov_b32 m0, s43
	v_mov_b32_e32 v185, v1
	global_load_lds_dwordx4 v184, s[30:31]
	s_barrier
	s_waitcnt lgkmcnt(0)
	v_lshl_add_u64 v[242:243], s[30:31], 0, v[0:1]
	v_lshl_add_u64 v[244:245], s[30:31], 0, v[184:185]
	s_waitcnt lgkmcnt(0)
	v_mfma_f32_16x16x32_bf16 v[62:65], v[130:133], v[146:149], v[62:65]
	v_mfma_f32_16x16x32_bf16 v[58:61], v[138:141], v[146:149], v[58:61]
	v_mfma_f32_16x16x32_bf16 v[46:49], v[130:133], v[154:157], v[46:49]
	v_mfma_f32_16x16x32_bf16 v[42:45], v[138:141], v[154:157], v[42:45]
	v_mfma_f32_16x16x32_bf16 v[30:33], v[130:133], v[162:165], v[30:33]
	v_mfma_f32_16x16x32_bf16 v[26:29], v[138:141], v[162:165], v[26:29]
	v_mfma_f32_16x16x32_bf16 v[14:17], v[130:133], v[170:173], v[14:17]
	v_mfma_f32_16x16x32_bf16 v[10:13], v[138:141], v[170:173], v[10:13]
	v_mfma_f32_16x16x32_bf16 v[62:65], v[134:137], v[150:153], v[62:65]
	v_mfma_f32_16x16x32_bf16 v[58:61], v[142:145], v[150:153], v[58:61]
	v_mfma_f32_16x16x32_bf16 v[46:49], v[134:137], v[158:161], v[46:49]
	v_mfma_f32_16x16x32_bf16 v[42:45], v[142:145], v[158:161], v[42:45]
	v_mfma_f32_16x16x32_bf16 v[30:33], v[134:137], v[166:169], v[30:33]
	v_mfma_f32_16x16x32_bf16 v[26:29], v[142:145], v[166:169], v[26:29]
	v_mfma_f32_16x16x32_bf16 v[14:17], v[134:137], v[174:177], v[14:17]
	v_mfma_f32_16x16x32_bf16 v[10:13], v[142:145], v[174:177], v[10:13]
	s_barrier
	v_lshl_add_u64 v[130:131], v[236:237], 0, s[90:91]
	s_add_i32 s4, s26, s38
	v_lshl_add_u64 v[132:133], v[130:131], 0, v[180:181]
	s_mov_b32 m0, s4
	v_lshl_add_u64 v[130:131], v[130:131], 0, v[182:183]
	global_load_lds_dwordx4 v[132:133], off
	s_add_i32 m0, s4, 0x2000
	s_nop 0
	global_load_lds_dwordx4 v[130:131], off
	s_waitcnt vmcnt(6)
	s_barrier
	v_mfma_f32_16x16x32_bf16 v[54:57], v[200:203], v[146:149], v[54:57]
	v_mfma_f32_16x16x32_bf16 v[50:53], v[210:213], v[146:149], v[50:53]
	v_mfma_f32_16x16x32_bf16 v[38:41], v[200:203], v[154:157], v[38:41]
	v_mfma_f32_16x16x32_bf16 v[34:37], v[210:213], v[154:157], v[34:37]
	v_mfma_f32_16x16x32_bf16 v[22:25], v[200:203], v[162:165], v[22:25]
	v_mfma_f32_16x16x32_bf16 v[18:21], v[210:213], v[162:165], v[18:21]
	v_mfma_f32_16x16x32_bf16 v[6:9], v[200:203], v[170:173], v[6:9]
	v_mfma_f32_16x16x32_bf16 v[2:5], v[210:213], v[170:173], v[2:5]
	v_mfma_f32_16x16x32_bf16 v[54:57], v[206:209], v[150:153], v[54:57]
	v_mfma_f32_16x16x32_bf16 v[50:53], v[232:235], v[150:153], v[50:53]
	v_mfma_f32_16x16x32_bf16 v[38:41], v[206:209], v[158:161], v[38:41]
	v_mfma_f32_16x16x32_bf16 v[34:37], v[232:235], v[158:161], v[34:37]
	v_mfma_f32_16x16x32_bf16 v[22:25], v[206:209], v[166:169], v[22:25]
	v_mfma_f32_16x16x32_bf16 v[18:21], v[232:235], v[166:169], v[18:21]
	v_mfma_f32_16x16x32_bf16 v[6:9], v[206:209], v[174:177], v[6:9]
	v_mfma_f32_16x16x32_bf16 v[2:5], v[232:235], v[174:177], v[2:5]
	s_add_i32 s4, 0, 0x18000
	v_add_u32_e32 v142, s4, v224
	s_barrier
	ds_read_b128 v[130:133], v142
	ds_read_b128 v[134:137], v142 offset:1024
	ds_read_b128 v[138:141], v142 offset:2048
	ds_read_b128 v[142:145], v142 offset:3072
	s_mov_b32 m0, s46
	v_lshl_add_u64 v[198:199], s[30:31], 0, v[198:199]
	ds_read_b128 v[146:149], v226 offset:32768
	ds_read_b128 v[150:153], v226 offset:33792
	ds_read_b128 v[154:157], v226 offset:34816
	ds_read_b128 v[158:161], v226 offset:35840
	ds_read_b128 v[162:165], v226 offset:36864
	ds_read_b128 v[166:169], v226 offset:37888
	ds_read_b128 v[170:173], v226 offset:38912
	ds_read_b128 v[174:177], v226 offset:39936
	global_load_lds_dwordx4 v[198:199], off
	v_lshl_add_u64 v[198:199], s[30:31], 0, v[188:189]
	s_mov_b32 m0, s47
	s_nop 0
	global_load_lds_dwordx4 v[198:199], off
	s_waitcnt lgkmcnt(8)
	s_barrier
; #define PG8_STAGE(bufoff, gbase, voff) do { _Pragma("unroll") for (int _i = 0; _i < 2; ++_i) \
;         __builtin_amdgcn_global_load_lds((const unsigned*)((const char*)(gbase) + (voff)[_i]), (LAS unsigned*)(lds + (bufoff) + ldsw + _i * 8192), 16, 0, 0); } while (0)
; #define PG8_LDA(dst, b, h) do { _Pragma("unroll") for (int m = 0; m < 4; ++m) _Pragma("unroll") for (int k = 0; k < 2; ++k) dst[m][k] = *(const LAS bf16x8*)(lds + PG8_SA(b, h) + aoff + m * 2048 + k * 1024); } while (0)
; #define PG8_LDB(dst, b, h) do { _Pragma("unroll") for (int n = 0; n < 2; ++n) _Pragma("unroll") for (int k = 0; k < 2; ++k) dst[n][k] = *(const LAS bf16x8*)(lds + PG8_SB(b, h) + boff + n * 2048 + k * 1024); } while (0)
; #define PG8_MMA(ai, bj, At, Bt) do { __builtin_amdgcn_s_setprio(1); _Pragma("unroll") for (int m = 0; m < 4; ++m) _Pragma("unroll") for (int n = 0; n < 2; ++n) _Pragma("unroll") for (int k = 0; k < 2; ++k) \
;         acc[ai][bj][m][n] = __builtin_amdgcn_mfma_f32_16x16x32_bf16(Bt[n][k], At[m][k], acc[ai][bj][m][n], 0, 0, 0); __builtin_amdgcn_s_setprio(0); } while (0)
; #define PG8_WAIT_V(n) asm volatile("s_waitcnt vmcnt(" #n ")" ::: "memory")
; #define PG8_WAIT_L(n) asm volatile("s_waitcnt lgkmcnt(" #n ")" ::: "memory")
; #define PG8_BAR __builtin_amdgcn_s_barrier()
; #define PG8_SCHED __builtin_amdgcn_sched_barrier(0)
; template <class Epi, class Sched>
; __device__ __forceinline__ void gemm_phase(LAS unsigned char* lds, const bf16_t* Abase, const int K, const Sched& S, const Epi& E, const int wvid) {
;     ...
;             PG8_WAIT_L(8); PG8_BAR; PG8_WAIT_L(0); PG8_MMA(0, 0, At, B0); PG8_BAR; PG8_SCHED;
;             PG8_LDB(B1, 1, 1); PG8_STAGE(PG8_SB(1, 0), b3, voffB);
;             PG8_BAR; PG8_WAIT_L(0); PG8_MMA(0, 1, At, B1); PG8_BAR;
;             PG8_LDA(At, 1, 1); PG8_STAGE(PG8_SA(1, 0), a3, voffA[0]);
;             PG8_BAR; PG8_WAIT_L(0); PG8_MMA(1, 0, At, B0); PG8_BAR; PG8_SCHED;
;             PG8_STAGE(PG8_SB(1, 1), b3 + hstep, voffB);
;             PG8_WAIT_V(6); PG8_BAR; PG8_MMA(1, 1, At, B1); PG8_BAR;
	s_waitcnt lgkmcnt(0)
	s_waitcnt lgkmcnt(0)
	v_mfma_f32_16x16x32_bf16 v[126:129], v[130:133], v[146:149], v[126:129]
	v_mfma_f32_16x16x32_bf16 v[122:125], v[138:141], v[146:149], v[122:125]
	v_mfma_f32_16x16x32_bf16 v[118:121], v[130:133], v[154:157], v[118:121]
	v_mfma_f32_16x16x32_bf16 v[114:117], v[138:141], v[154:157], v[114:117]
	v_mfma_f32_16x16x32_bf16 v[110:113], v[130:133], v[162:165], v[110:113]
	v_mfma_f32_16x16x32_bf16 v[106:109], v[138:141], v[162:165], v[106:109]
	v_mfma_f32_16x16x32_bf16 v[94:97], v[130:133], v[170:173], v[94:97]
	v_mfma_f32_16x16x32_bf16 v[90:93], v[138:141], v[170:173], v[90:93]
	v_mfma_f32_16x16x32_bf16 v[126:129], v[134:137], v[150:153], v[126:129]
	v_mfma_f32_16x16x32_bf16 v[122:125], v[142:145], v[150:153], v[122:125]
	v_mfma_f32_16x16x32_bf16 v[118:121], v[134:137], v[158:161], v[118:121]
	v_mfma_f32_16x16x32_bf16 v[114:117], v[142:145], v[158:161], v[114:117]
	v_mfma_f32_16x16x32_bf16 v[110:113], v[134:137], v[166:169], v[110:113]
	v_mfma_f32_16x16x32_bf16 v[106:109], v[142:145], v[166:169], v[106:109]
	v_mfma_f32_16x16x32_bf16 v[94:97], v[134:137], v[174:177], v[94:97]
	v_mfma_f32_16x16x32_bf16 v[90:93], v[142:145], v[174:177], v[90:93]
	s_barrier
	s_add_i32 s5, 0, 0x1c000
	s_add_i32 s4, s4, s38
	v_add_u32_e32 v185, s5, v224
	v_lshl_add_u64 v[202:203], v[238:239], 0, s[12:13]
	s_mov_b32 m0, s4
	ds_read_b128 v[198:201], v185
	ds_read_b128 v[206:209], v185 offset:1024
	ds_read_b128 v[210:213], v185 offset:2048
	ds_read_b128 v[232:235], v185 offset:3072
	global_load_lds_dwordx4 v[202:203], off
	v_lshl_add_u64 v[202:203], v[240:241], 0, s[12:13]
	s_add_i32 m0, s4, 0x2000
	s_nop 0
	global_load_lds_dwordx4 v[202:203], off
	s_barrier
	s_waitcnt lgkmcnt(0)
	s_waitcnt lgkmcnt(0)
	v_mfma_f32_16x16x32_bf16 v[102:105], v[198:201], v[146:149], v[102:105]
	v_mfma_f32_16x16x32_bf16 v[98:101], v[210:213], v[146:149], v[98:101]
	v_mfma_f32_16x16x32_bf16 v[86:89], v[198:201], v[154:157], v[86:89]
	v_mfma_f32_16x16x32_bf16 v[82:85], v[210:213], v[154:157], v[82:85]
	v_mfma_f32_16x16x32_bf16 v[78:81], v[198:201], v[162:165], v[78:81]
	v_mfma_f32_16x16x32_bf16 v[74:77], v[210:213], v[162:165], v[74:77]
	v_mfma_f32_16x16x32_bf16 v[70:73], v[198:201], v[170:173], v[70:73]
	v_mfma_f32_16x16x32_bf16 v[66:69], v[210:213], v[170:173], v[66:69]
	v_mfma_f32_16x16x32_bf16 v[102:105], v[206:209], v[150:153], v[102:105]
	v_mfma_f32_16x16x32_bf16 v[98:101], v[232:235], v[150:153], v[98:101]
	v_mfma_f32_16x16x32_bf16 v[86:89], v[206:209], v[158:161], v[86:89]
	v_mfma_f32_16x16x32_bf16 v[82:85], v[232:235], v[158:161], v[82:85]
	v_mfma_f32_16x16x32_bf16 v[78:81], v[206:209], v[166:169], v[78:81]
	v_mfma_f32_16x16x32_bf16 v[74:77], v[232:235], v[166:169], v[74:77]
	v_mfma_f32_16x16x32_bf16 v[70:73], v[206:209], v[174:177], v[70:73]
	v_mfma_f32_16x16x32_bf16 v[66:69], v[232:235], v[174:177], v[66:69]
	s_mov_b32 m0, s48
	v_lshl_add_u64 v[202:203], v[242:243], 0, s[12:13]
	s_barrier
	ds_read_b128 v[146:149], v226 offset:49152
	ds_read_b128 v[150:153], v226 offset:50176
	ds_read_b128 v[154:157], v226 offset:51200
	ds_read_b128 v[158:161], v226 offset:52224
	ds_read_b128 v[162:165], v226 offset:53248
	ds_read_b128 v[166:169], v226 offset:54272
	ds_read_b128 v[170:173], v226 offset:55296
	ds_read_b128 v[174:177], v226 offset:56320
	global_load_lds_dwordx4 v[202:203], off
	v_lshl_add_u64 v[202:203], v[244:245], 0, s[12:13]
	s_mov_b32 m0, s49
	s_nop 0
	global_load_lds_dwordx4 v[202:203], off
	s_barrier
	s_waitcnt lgkmcnt(0)
	s_waitcnt lgkmcnt(0)
	v_mfma_f32_16x16x32_bf16 v[62:65], v[130:133], v[146:149], v[62:65]
	v_mfma_f32_16x16x32_bf16 v[58:61], v[138:141], v[146:149], v[58:61]
	v_mfma_f32_16x16x32_bf16 v[46:49], v[130:133], v[154:157], v[46:49]
	v_mfma_f32_16x16x32_bf16 v[42:45], v[138:141], v[154:157], v[42:45]
	v_mfma_f32_16x16x32_bf16 v[30:33], v[130:133], v[162:165], v[30:33]
	v_mfma_f32_16x16x32_bf16 v[26:29], v[138:141], v[162:165], v[26:29]
	v_mfma_f32_16x16x32_bf16 v[14:17], v[130:133], v[170:173], v[14:17]
	v_mfma_f32_16x16x32_bf16 v[10:13], v[138:141], v[170:173], v[10:13]
	v_mfma_f32_16x16x32_bf16 v[62:65], v[134:137], v[150:153], v[62:65]
	v_mfma_f32_16x16x32_bf16 v[58:61], v[142:145], v[150:153], v[58:61]
	v_mfma_f32_16x16x32_bf16 v[46:49], v[134:137], v[158:161], v[46:49]
	v_mfma_f32_16x16x32_bf16 v[42:45], v[142:145], v[158:161], v[42:45]
	v_mfma_f32_16x16x32_bf16 v[30:33], v[134:137], v[166:169], v[30:33]
	v_mfma_f32_16x16x32_bf16 v[26:29], v[142:145], v[166:169], v[26:29]
	v_mfma_f32_16x16x32_bf16 v[14:17], v[134:137], v[174:177], v[14:17]
	v_mfma_f32_16x16x32_bf16 v[10:13], v[142:145], v[174:177], v[10:13]
	s_barrier
	v_lshl_add_u64 v[130:131], v[236:237], 0, s[14:15]
	s_add_i32 s4, s5, s38
	v_lshl_add_u64 v[132:133], v[130:131], 0, v[180:181]
	s_mov_b32 m0, s4
	v_lshl_add_u64 v[130:131], v[130:131], 0, v[182:183]
	global_load_lds_dwordx4 v[132:133], off
	s_add_i32 m0, s4, 0x2000
	s_nop 0
	global_load_lds_dwordx4 v[130:131], off
	s_waitcnt vmcnt(6)
	s_barrier
	v_mfma_f32_16x16x32_bf16 v[54:57], v[198:201], v[146:149], v[54:57]
	v_mfma_f32_16x16x32_bf16 v[50:53], v[210:213], v[146:149], v[50:53]
	v_mfma_f32_16x16x32_bf16 v[38:41], v[198:201], v[154:157], v[38:41]
	v_mfma_f32_16x16x32_bf16 v[34:37], v[210:213], v[154:157], v[34:37]
	v_mfma_f32_16x16x32_bf16 v[22:25], v[198:201], v[162:165], v[22:25]
	v_mfma_f32_16x16x32_bf16 v[18:21], v[210:213], v[162:165], v[18:21]
	v_mfma_f32_16x16x32_bf16 v[6:9], v[198:201], v[170:173], v[6:9]
	v_mfma_f32_16x16x32_bf16 v[2:5], v[210:213], v[170:173], v[2:5]
	v_mfma_f32_16x16x32_bf16 v[54:57], v[206:209], v[150:153], v[54:57]
	v_mfma_f32_16x16x32_bf16 v[50:53], v[232:235], v[150:153], v[50:53]
	v_mfma_f32_16x16x32_bf16 v[38:41], v[206:209], v[158:161], v[38:41]
	v_mfma_f32_16x16x32_bf16 v[34:37], v[232:235], v[158:161], v[34:37]
	v_mfma_f32_16x16x32_bf16 v[22:25], v[206:209], v[166:169], v[22:25]
	v_mfma_f32_16x16x32_bf16 v[18:21], v[232:235], v[166:169], v[18:21]
	v_mfma_f32_16x16x32_bf16 v[6:9], v[206:209], v[174:177], v[6:9]
	v_mfma_f32_16x16x32_bf16 v[2:5], v[232:235], v[174:177], v[2:5]
	s_add_i32 s23, s23, 2
	s_cmp_gt_u32 s23, 13
	s_cbranch_scc1 .Lx_g1
	s_barrier
	s_mov_b64 s[26:27], s[28:29]
	s_branch .LBB0_1209

; __device__ __forceinline__ unsigned cvt_pk_bf16(float lo, float hi) { f32x2c v = {lo, hi}; bf16x2c b = __builtin_convertvector(v, bf16x2c); return __builtin_bit_cast(unsigned, b); }
;     __device__ __forceinline__ void operator()(const f32x4 (&acc)[2][2][4][2], const Unit& u, int wr, int wc, int fr, int fq) const {
;         const int row0 = u.row0 + wr * 64 + fr, col0 = (u.pn * BM + wc * 32 + 8 * fq) >> 1;
;         const int odd = fq & 1;
; #pragma unroll
;         for (int ai = 0; ai < 2; ++ai)
; #pragma unroll
;             for (int m = 0; m < 4; ++m) { const int row = row0 + ai * HALF + m * 16; bf16_t* rowp = A + (size_t)row * FF + col0;
;                 u32x2 w[2];
; #pragma unroll
;                 for (int bj = 0; bj < 2; ++bj) { const f32x4 a = acc[ai][bj][m][0], b = acc[ai][bj][m][1]; float o[4];
; #pragma unroll
;                     for (int j = 0; j < 4; ++j) o[j] = a[j] * __builtin_amdgcn_rcpf(1.0f + __expf(-a[j])) * b[j];
;                     w[bj].x = cvt_pk_bf16(o[0], o[1]); w[bj].y = cvt_pk_bf16(o[2], o[3]); }
;                 const auto rx = __builtin_amdgcn_permlane16_swap(w[0].x, w[1].x, false, false); const auto ry = __builtin_amdgcn_permlane16_swap(w[0].y, w[1].y, false, false);
;                 u32x4 v; v.x = rx[0]; v.y = ry[0]; v.z = rx[1]; v.w = ry[1];
;                 if (row < u.rend) *(u32x4*)(rowp + (odd ? HALF / 2 - 4 : 0)) = v; }
.Lxa1:
.LBB0_1214:
	v_mul_f32_e32 v133, 0xbfb8aa3b, v126
	v_exp_f32_e32 v133, v133
	v_lshl_or_b32 v130, s24, 8, v225
	v_ashrrev_i32_e32 v130, 1, v130
	v_add_u32_e32 v132, v228, v223
	v_add_f32_e32 v133, 1.0, v133
	v_rcp_f32_e32 v134, v133
	v_mul_f32_e32 v133, 0xbfb8aa3b, v127
	v_exp_f32_e32 v133, v133
	v_ashrrev_i32_e32 v131, 31, v130
	v_cmp_lt_i32_e32 vcc, v132, v179
	v_add_f32_e32 v133, 1.0, v133
	v_rcp_f32_e32 v135, v133
	s_nop 0
	v_pk_mul_f32 v[126:127], v[126:127], v[134:135]
	s_nop 0
	v_pk_mul_f32 v[122:123], v[122:123], v[126:127]
	v_mul_f32_e32 v126, 0xbfb8aa3b, v128
	v_mul_f32_e32 v127, 0xbfb8aa3b, v129
	v_exp_f32_e32 v126, v126
	v_exp_f32_e32 v127, v127
	v_cvt_pk_bf16_f32 v122, v122, v123
	v_add_f32_e32 v126, 1.0, v126
	v_add_f32_e32 v127, 1.0, v127
	v_rcp_f32_e32 v126, v126
	v_rcp_f32_e32 v127, v127
	s_nop 0
	v_pk_mul_f32 v[126:127], v[128:129], v[126:127]
	s_nop 0
	v_pk_mul_f32 v[124:125], v[124:125], v[126:127]
	s_nop 0
	v_cvt_pk_bf16_f32 v123, v124, v125
	v_mul_f32_e32 v124, 0xbfb8aa3b, v102
	v_mul_f32_e32 v125, 0xbfb8aa3b, v103
	v_exp_f32_e32 v124, v124
	v_exp_f32_e32 v125, v125
	v_add_f32_e32 v124, 1.0, v124
	v_add_f32_e32 v125, 1.0, v125
	v_rcp_f32_e32 v124, v124
	v_rcp_f32_e32 v125, v125
	s_nop 0
	v_pk_mul_f32 v[102:103], v[102:103], v[124:125]
	s_nop 0
	v_pk_mul_f32 v[98:99], v[98:99], v[102:103]
	v_mul_f32_e32 v102, 0xbfb8aa3b, v104
	v_mul_f32_e32 v103, 0xbfb8aa3b, v105
	v_exp_f32_e32 v102, v102
	v_exp_f32_e32 v103, v103
	v_cvt_pk_bf16_f32 v124, v98, v99
	s_nop 1
	v_permlane16_swap_b32_e32 v122, v124
	v_add_f32_e32 v102, 1.0, v102
	v_add_f32_e32 v103, 1.0, v103
	v_rcp_f32_e32 v102, v102
	v_rcp_f32_e32 v103, v103
	s_nop 0
	v_pk_mul_f32 v[102:103], v[104:105], v[102:103]
	s_nop 0
	v_pk_mul_f32 v[100:101], v[100:101], v[102:103]
	v_lshlrev_b32_e32 v102, 1, v178
	v_cvt_pk_bf16_f32 v125, v100, v101
	s_nop 1
	v_permlane16_swap_b32_e32 v123, v125
	s_and_saveexec_b64 s[0:1], vcc
	s_cbranch_execz .LBB0_1216
	v_ashrrev_i32_e32 v133, 31, v132
	v_lshlrev_b64 v[98:99], 10, v[132:133]
	v_lshl_add_u64 v[98:99], s[18:19], 0, v[98:99]
	v_lshl_add_u64 v[98:99], v[130:131], 1, v[98:99]
	v_mov_b32_e32 v103, v1
	v_lshl_add_u64 v[98:99], v[98:99], 0, v[102:103]
	global_store_dwordx4 v[98:99], v[122:125], off

; template <class Epi, class Sched>
; __device__ __forceinline__ void gemm_phase(LAS unsigned char* lds, const bf16_t* Abase, const int K, const Sched& S, const Epi& E, const int wvid) {
;     ...
;         E(acc, cur, wr, wc, fr, fq);
;         if (!has_next) break;
; #pragma unroll
;         for (int a = 0; a < 2; ++a)
; #pragma unroll
;             for (int b = 0; b < 2; ++b)
; #pragma unroll
;                 for (int m = 0; m < 4; ++m)
; #pragma unroll
;                     for (int n = 0; n < 2; ++n) acc[a][b][m][n] = (f32x4){0.f, 0.f, 0.f, 0.f};
;         cur = nxt; cB = nB; ++ui;
.Lxb2:
	s_and_b64 vcc, exec, s[2:3]
	v_mov_b32_e32 v227, v228
	s_mov_b32 s16, s24
	v_mov_b32_e32 v179, v193
	v_mov_b32_e32 v226, v192
	v_mov_b64_e32 v[2:3], v[194:195]
	s_cbranch_vccnz .LBB0_1497

;     __device__ __forceinline__ void operator()(const f32x4 (&acc)[2][2][4][2], const Unit& u, int wr, int wc, int fr, int fq) const {
;     ...
;         float gt[2][4];
; #pragma unroll
;         for (int ai = 0; ai < 2; ++ai)
; #pragma unroll
;             for (int m = 0; m < 4; ++m) gt[ai][m] = gate[u.loff + min(row0 + ai * HALF + m * 16, u.rend - 1)];
; #pragma unroll
;         for (int ai = 0; ai < 2; ++ai)
; #pragma unroll
;             for (int m = 0; m < 4; ++m) { const int row = row0 + ai * HALF + m * 16; if (row < u.rend) { const float g = gt[ai][m]; bf16_t* rowp = Y + (size_t)row * D + col0;
.Lg2x:
	v_add_u32_e32 v160, v227, v178
	v_add_u32_e32 v133, -1, v179
	v_add_u32_e32 v158, 16, v160
	v_min_i32_e32 v130, v158, v133
	v_add_u32_e32 v130, v226, v130
	v_ashrrev_i32_e32 v131, 31, v130
	v_lshl_add_u64 v[130:131], v[130:131], 2, s[20:21]
	v_add_u32_e32 v154, 32, v160
	global_load_dword v156, v[130:131], off
	v_min_i32_e32 v130, v154, v133
	v_add_u32_e32 v130, v226, v130
	v_ashrrev_i32_e32 v131, 31, v130
	v_lshl_add_u64 v[130:131], v[130:131], 2, s[20:21]
	v_add_u32_e32 v150, 48, v160
	global_load_dword v152, v[130:131], off
	v_min_i32_e32 v130, v150, v133
	v_add_u32_e32 v130, v226, v130
	v_ashrrev_i32_e32 v131, 31, v130
	v_lshl_add_u64 v[130:131], v[130:131], 2, s[20:21]
	v_add_u32_e32 v146, 0x80, v160
	global_load_dword v148, v[130:131], off
	v_min_i32_e32 v130, v146, v133
	v_add_u32_e32 v130, v226, v130
	v_ashrrev_i32_e32 v131, 31, v130
	v_lshl_add_u64 v[130:131], v[130:131], 2, s[20:21]
	v_add_u32_e32 v142, 0x90, v160
	global_load_dword v144, v[130:131], off
	v_min_i32_e32 v130, v142, v133
	v_add_u32_e32 v130, v226, v130
	v_ashrrev_i32_e32 v131, 31, v130
	v_lshl_add_u64 v[130:131], v[130:131], 2, s[20:21]
	v_add_u32_e32 v138, 0xa0, v160
	global_load_dword v140, v[130:131], off
	v_min_i32_e32 v130, v138, v133
	v_add_u32_e32 v130, v226, v130
	v_ashrrev_i32_e32 v131, 31, v130
	v_lshl_add_u64 v[130:131], v[130:131], 2, s[20:21]
	v_add_u32_e32 v132, 0xb0, v160
	global_load_dword v134, v[130:131], off
	v_min_i32_e32 v130, v132, v133
	v_add_u32_e32 v130, v226, v130
	v_ashrrev_i32_e32 v131, 31, v130
	v_lshl_add_u64 v[130:131], v[130:131], 2, s[20:21]
	global_load_dword v130, v[130:131], off
	s_cmp_lt_u32 s74, 0x100
	s_cbranch_scc0 .Lxa2
	s_barrier
.Lxa2:
.LBB0_1481:
	v_lshl_or_b32 v136, s16, 8, v224
	v_ashrrev_i32_e32 v137, 31, v136
	v_cmp_lt_i32_e32 vcc, v160, v179
	s_and_saveexec_b64 s[0:1], vcc
	s_cbranch_execnz .LBB0_1489
	s_or_b64 exec, exec, s[0:1]
	v_cmp_lt_i32_e32 vcc, v158, v179
	s_and_saveexec_b64 s[0:1], vcc
	s_cbranch_execnz .LBB0_1490
